# v65 + in-proj tile order: LayerNorm-statistics gelu tiles (2,3) swapped with the plain tiles (8,9): converting workgroups get plain+rope+2 sigmoid
# baseline (speedup 1.0000x reference)
;     __device__ bool next(int i, Unit& u) const { if (!base.next(i >> 1, u)) return false; if (i & 1) { u.pm += MTOK / BM; u.pn += DM / BM; } return true; }
;   __device__ __forceinline__ bool next(int i,AttnUnit&u)const{ if(i>=2||vcu>=256)return false; const int s=vcu&3; u.bh=vcu>>2; u.qb=(i==0)?7-s:s; return true; }
;     __host__ __device__ bool next(int i, Unit& u) const {
;         const int L = i * G + c; if (L >= nwg) return false;
;         int wgid = L; { const int q = nwg / NXCD, r = nwg % NXCD, xcd = wgid % NXCD, off = wgid / NXCD; wgid = (xcd < r ? xcd * (q + 1) : r * (q + 1) + (xcd - r) * q) + off; }
;         const int nig = WGM * nN, gid = wgid / nig, fm = gid * WGM, gsz = (nM - fm) < WGM ? (nM - fm) : WGM;
;         u.pm = fm + ((wgid % nig) % gsz); u.pn = (wgid % nig) / gsz; u.half = 0; return true;
.LBB0_382:
	s_ashr_i32 s4, s21, 31
	s_lshr_b32 s4, s4, 29
	s_add_i32 s4, s21, s4
	s_ashr_i32 s5, s4, 3
	s_and_b32 s4, s4, -8
	s_sub_i32 s4, s21, s4
	s_cmp_lt_i32 s4, 0
	s_movk_i32 s6, 0x91
	s_cselect_b32 s6, s6, 0x90
	s_mul_i32 s4, s4, s6
	s_add_i32 s4, s4, s5
	s_mul_hi_i32 s5, s4, 0x38e38e39
	s_lshr_b32 s6, s5, 31
	s_ashr_i32 s5, s5, 5
	s_add_i32 s5, s5, s6
	s_lshl_b32 s6, s5, 3
	s_mulk_i32 s5, 0x90
	s_sub_i32 s4, s4, s5
	s_bfe_u32 s5, s4, 0x3001c
	s_add_i32 s5, s4, s5
	s_sext_i32_i16 s7, s5
	s_and_b32 s5, s5, 0xfff8
	s_sub_i32 s4, s4, s5
	s_sext_i32_i16 s4, s4
	s_add_i32 s18, s6, s4
	s_ashr_i32 s70, s7, 3
	s_mul_i32 s4, s70, 5
	s_cmp_lt_u32 s70, 12
	s_cbranch_scc0 .Lpn_hi0
	s_mov_b32 s6, 0x8a44a020
	s_mov_b32 s7, 0x5a86239
	s_branch .Lpn_go0

;     __device__ bool next(int i, Unit& u) const { if (!base.next(i >> 1, u)) return false; if (i & 1) { u.pm += MTOK / BM; u.pn += DM / BM; } return true; }
;   __device__ __forceinline__ bool next(int i,AttnUnit&u)const{ if(i>=2||vcu>=256)return false; const int s=vcu&3; u.bh=vcu>>2; u.qb=(i==0)?7-s:s; return true; }
;     __host__ __device__ bool next(int i, Unit& u) const {
;         const int L = i * G + c; if (L >= nwg) return false;
;         int wgid = L; { const int q = nwg / NXCD, r = nwg % NXCD, xcd = wgid % NXCD, off = wgid / NXCD; wgid = (xcd < r ? xcd * (q + 1) : r * (q + 1) + (xcd - r) * q) + off; }
;         const int nig = WGM * nN, gid = wgid / nig, fm = gid * WGM, gsz = (nM - fm) < WGM ? (nM - fm) : WGM;
;         u.pm = fm + ((wgid % nig) % gsz); u.pn = (wgid % nig) / gsz; u.half = 0; return true;
; template <class Epi, class Sched, bool ALIGN_EPI = false, bool SP2 = false>
; __device__ __forceinline__ void gemm_phase(PG8_LAS unsigned char* lds, const Gemm g, const Sched& S, const Epi& E) {
;     ...
;         const bool has_next = S.next(ui + 1, nxt);
;         const char* nA = has_next ? (const char*)g.A + (size_t)nxt.pm * tstep + (nxt.half == 2 ? hstep : (size_t)0) : cA; const char* nB = has_next ? (const char*)g.Bt + (size_t)nxt.pn * tstep : cB;
.LBB0_392:
	s_add_i32 s72, s72, 1
	s_mul_i32 s10, s72, s33
	s_add_i32 s10, s10, s21
	s_cmpk_lt_i32 s10, 0x480
	s_cselect_b64 s[64:65], -1, 0
	s_cmpk_gt_i32 s10, 0x47f
	s_cbranch_scc1 .LBB0_394
	s_ashr_i32 s11, s10, 31
	s_lshr_b32 s11, s11, 29
	s_add_i32 s11, s10, s11
	s_ashr_i32 s12, s11, 3
	s_and_b32 s11, s11, -8
	s_sub_i32 s10, s10, s11
	s_cmp_lt_i32 s10, 0
	s_movk_i32 s11, 0x91
	s_cselect_b32 s11, s11, 0x90
	s_mul_i32 s10, s10, s11
	s_add_i32 s10, s10, s12
	s_mul_hi_i32 s11, s10, 0x38e38e39
	s_lshr_b32 s12, s11, 31
	s_ashr_i32 s11, s11, 5
	s_add_i32 s11, s11, s12
	s_lshl_b32 s12, s11, 3
	s_mulk_i32 s11, 0x90
	s_sub_i32 s10, s10, s11
	s_bfe_u32 s11, s10, 0x3001c
	s_add_i32 s11, s10, s11
	s_sext_i32_i16 s13, s11
	s_and_b32 s11, s11, 0xfff8
	s_sub_i32 s10, s10, s11
	s_sext_i32_i16 s10, s10
	s_add_i32 s60, s12, s10
	s_ashr_i32 s62, s13, 3
	s_mul_i32 s10, s62, 5
	s_cmp_lt_u32 s62, 12
	s_cbranch_scc0 .Lpn_hi1
	s_mov_b32 s12, 0x8a44a020
	s_mov_b32 s13, 0x5a86239
	s_branch .Lpn_go1
